# v10 plus DSA fast path softmax regenerated with packed f32 ops (v_pk_fma_f32 exponent, v_pk_add_f32 row sum)
# speedup vs baseline: 1.0037x; 1.0037x over previous
.Lmy_dsa_fast_nk_skip:
	v_lshl_add_u32 v151, v247, 1, s19
	ds_read_u16 v46, v151
	ds_read_u16 v47, v151 offset:16
	ds_read_u16 v126, v151 offset:32
	ds_read_u16 v127, v151 offset:48
	s_waitcnt lgkmcnt(0)
	v_lshl_or_b32 v46, v46, 8, v250
	v_lshl_or_b32 v47, v47, 8, v250
	global_load_dwordx4 v[102:105], v46, s[50:51] offset:128
	global_load_dwordx4 v[110:113], v47, s[50:51] offset:128
	v_lshl_or_b32 v46, v126, 8, v250
	v_lshl_or_b32 v47, v127, 8, v250
	global_load_dwordx4 v[126:129], v46, s[50:51] offset:128
	global_load_dwordx4 v[130:133], v47, s[50:51] offset:128
	ds_read_u16 v46, v151 offset:64
	ds_read_u16 v47, v151 offset:80
	ds_read_u16 v118, v151 offset:96
	ds_read_u16 v119, v151 offset:112
	s_waitcnt lgkmcnt(0)
	v_lshl_or_b32 v46, v46, 8, v250
	v_lshl_or_b32 v47, v47, 8, v250
	global_load_dwordx4 v[86:89], v46, s[50:51] offset:128
	global_load_dwordx4 v[94:97], v47, s[50:51] offset:128
	v_lshl_or_b32 v46, v118, 8, v250
	v_lshl_or_b32 v47, v119, 8, v250
	global_load_dwordx4 v[118:121], v46, s[50:51] offset:128
	global_load_dwordx4 v[122:125], v47, s[50:51] offset:128
	ds_read_u16 v46, v151 offset:128
	ds_read_u16 v47, v151 offset:144
	ds_read_u16 v106, v151 offset:160
	ds_read_u16 v107, v151 offset:176
	s_waitcnt lgkmcnt(0)
	v_lshl_or_b32 v46, v46, 8, v250
	v_lshl_or_b32 v47, v47, 8, v250
	global_load_dwordx4 v[78:81], v46, s[50:51] offset:128
	global_load_dwordx4 v[82:85], v47, s[50:51] offset:128
	v_lshl_or_b32 v46, v106, 8, v250
	v_lshl_or_b32 v47, v107, 8, v250
	global_load_dwordx4 v[106:109], v46, s[50:51] offset:128
	global_load_dwordx4 v[114:117], v47, s[50:51] offset:128
	ds_read_u16 v46, v151 offset:192
	ds_read_u16 v47, v151 offset:208
	ds_read_u16 v90, v151 offset:224
	ds_read_u16 v91, v151 offset:240
	s_waitcnt lgkmcnt(0)
	v_lshl_or_b32 v46, v46, 8, v250
	v_lshl_or_b32 v47, v47, 8, v250
	global_load_dwordx4 v[70:73], v46, s[50:51] offset:128
	global_load_dwordx4 v[74:77], v47, s[50:51] offset:128
	v_lshl_or_b32 v46, v90, 8, v250
	v_lshl_or_b32 v47, v91, 8, v250
	global_load_dwordx4 v[90:93], v46, s[50:51] offset:128
	global_load_dwordx4 v[98:101], v47, s[50:51] offset:128
	v_mov_b32_e32 v46, v49
	s_nop 1
	v_permlane32_swap_b32 v49, v46
	s_nop 1
	s_nop 0
	v_max_f32_e32 v46, v46, v46
	v_max_f32_e32 v47, v49, v49
	v_max_f32_e32 v46, v47, v46
	v_mov_b32_e32 v47, v46
	s_nop 1
	v_permlane16_swap_b32 v46, v47
	s_nop 1
	s_nop 0
	v_max_f32_e32 v47, v47, v47
	v_max_f32_e32 v46, v46, v46
	v_max_f32_e32 v49, v46, v47
	s_mov_b32 s32, 0x3fb8aa3b
	v_mul_f32_e32 v49, 0xbfb8aa3b, v49
	v_mov_b32_e32 v48, v49
	v_pk_fma_f32 v[226:227], v[158:159], s[32:33], v[48:49] op_sel_hi:[1,0,1]
	v_pk_fma_f32 v[158:159], v[44:45], s[32:33], v[48:49] op_sel_hi:[1,0,1]
	v_exp_f32_e32 v226, v226
	v_exp_f32_e32 v227, v227
	v_pk_fma_f32 v[228:229], v[156:157], s[32:33], v[48:49] op_sel_hi:[1,0,1]
	v_exp_f32_e32 v158, v158
	v_exp_f32_e32 v159, v159
	v_pk_fma_f32 v[230:231], v[160:161], s[32:33], v[48:49] op_sel_hi:[1,0,1]
	v_exp_f32_e32 v228, v228
	v_exp_f32_e32 v229, v229
	v_pk_add_f32 v[44:45], v[226:227], v[158:159]
	v_pk_fma_f32 v[232:233], v[154:155], s[32:33], v[48:49] op_sel_hi:[1,0,1]
	v_exp_f32_e32 v230, v230
	v_exp_f32_e32 v231, v231
	v_pk_add_f32 v[44:45], v[228:229], v[44:45]
	v_pk_fma_f32 v[218:219], v[166:167], s[32:33], v[48:49] op_sel_hi:[1,0,1]
	v_exp_f32_e32 v232, v232
	v_exp_f32_e32 v233, v233
	v_pk_add_f32 v[44:45], v[230:231], v[44:45]
	v_pk_fma_f32 v[220:221], v[164:165], s[32:33], v[48:49] op_sel_hi:[1,0,1]
	v_exp_f32_e32 v218, v218
	v_exp_f32_e32 v219, v219
	v_pk_add_f32 v[44:45], v[232:233], v[44:45]
	v_pk_fma_f32 v[222:223], v[168:169], s[32:33], v[48:49] op_sel_hi:[1,0,1]
	v_exp_f32_e32 v220, v220
	v_exp_f32_e32 v221, v221
	v_pk_add_f32 v[44:45], v[218:219], v[44:45]
	v_pk_fma_f32 v[224:225], v[162:163], s[32:33], v[48:49] op_sel_hi:[1,0,1]
	v_exp_f32_e32 v222, v222
	v_exp_f32_e32 v223, v223
	v_pk_add_f32 v[44:45], v[220:221], v[44:45]
	v_pk_fma_f32 v[206:207], v[174:175], s[32:33], v[48:49] op_sel_hi:[1,0,1]
	v_exp_f32_e32 v224, v224
	v_exp_f32_e32 v225, v225
	v_pk_add_f32 v[44:45], v[222:223], v[44:45]
	v_pk_fma_f32 v[208:209], v[172:173], s[32:33], v[48:49] op_sel_hi:[1,0,1]
	v_exp_f32_e32 v206, v206
	v_exp_f32_e32 v207, v207
	v_pk_add_f32 v[44:45], v[224:225], v[44:45]
	v_pk_fma_f32 v[46:47], v[142:143], s[32:33], v[48:49] op_sel_hi:[1,0,1]
	v_exp_f32_e32 v208, v208
	v_exp_f32_e32 v209, v209
	v_pk_add_f32 v[44:45], v[206:207], v[44:45]
	v_pk_fma_f32 v[134:135], v[140:141], s[32:33], v[48:49] op_sel_hi:[1,0,1]
	v_exp_f32_e32 v46, v46
	v_exp_f32_e32 v47, v47
	v_pk_add_f32 v[44:45], v[208:209], v[44:45]
	v_pk_fma_f32 v[214:215], v[176:177], s[32:33], v[48:49] op_sel_hi:[1,0,1]
	v_exp_f32_e32 v134, v134
	v_exp_f32_e32 v135, v135
	v_pk_add_f32 v[44:45], v[46:47], v[44:45]
	v_pk_fma_f32 v[216:217], v[170:171], s[32:33], v[48:49] op_sel_hi:[1,0,1]
	v_exp_f32_e32 v214, v214
	v_exp_f32_e32 v215, v215
	v_pk_add_f32 v[44:45], v[134:135], v[44:45]
	v_pk_fma_f32 v[136:137], v[144:145], s[32:33], v[48:49] op_sel_hi:[1,0,1]
	v_exp_f32_e32 v216, v216
	v_exp_f32_e32 v217, v217
	v_pk_add_f32 v[44:45], v[214:215], v[44:45]
	v_pk_fma_f32 v[182:183], v[182:183], s[32:33], v[48:49] op_sel_hi:[1,0,1]
	v_exp_f32_e32 v136, v136
	v_exp_f32_e32 v137, v137
	v_pk_add_f32 v[44:45], v[216:217], v[44:45]
	v_pk_fma_f32 v[138:139], v[138:139], s[32:33], v[48:49] op_sel_hi:[1,0,1]
	v_exp_f32_e32 v182, v182
	v_exp_f32_e32 v183, v183
	v_pk_add_f32 v[44:45], v[136:137], v[44:45]
	v_pk_fma_f32 v[180:181], v[180:181], s[32:33], v[48:49] op_sel_hi:[1,0,1]
	v_exp_f32_e32 v138, v138
	v_exp_f32_e32 v139, v139
	v_pk_add_f32 v[44:45], v[182:183], v[44:45]
	v_pk_fma_f32 v[184:185], v[184:185], s[32:33], v[48:49] op_sel_hi:[1,0,1]
	v_exp_f32_e32 v180, v180
	v_exp_f32_e32 v181, v181
	v_pk_add_f32 v[44:45], v[138:139], v[44:45]
	v_pk_fma_f32 v[196:197], v[178:179], s[32:33], v[48:49] op_sel_hi:[1,0,1]
	v_exp_f32_e32 v184, v184
	v_exp_f32_e32 v185, v185
	v_pk_add_f32 v[44:45], v[180:181], v[44:45]
	v_pk_fma_f32 v[172:173], v[190:191], s[32:33], v[48:49] op_sel_hi:[1,0,1]
	v_exp_f32_e32 v196, v196
	v_exp_f32_e32 v197, v197
	v_pk_add_f32 v[44:45], v[184:185], v[44:45]
	v_pk_fma_f32 v[174:175], v[188:189], s[32:33], v[48:49] op_sel_hi:[1,0,1]
	v_exp_f32_e32 v172, v172
	v_exp_f32_e32 v173, v173
	v_pk_add_f32 v[44:45], v[196:197], v[44:45]
	v_pk_fma_f32 v[176:177], v[192:193], s[32:33], v[48:49] op_sel_hi:[1,0,1]
	v_exp_f32_e32 v174, v174
	v_exp_f32_e32 v175, v175
	v_pk_add_f32 v[44:45], v[172:173], v[44:45]
	v_pk_fma_f32 v[178:179], v[186:187], s[32:33], v[48:49] op_sel_hi:[1,0,1]
	v_exp_f32_e32 v176, v176
	v_exp_f32_e32 v177, v177
	v_pk_add_f32 v[44:45], v[174:175], v[44:45]
	v_pk_fma_f32 v[164:165], v[200:201], s[32:33], v[48:49] op_sel_hi:[1,0,1]
	v_exp_f32_e32 v178, v178
	v_exp_f32_e32 v179, v179
	v_pk_add_f32 v[44:45], v[176:177], v[44:45]
	v_pk_fma_f32 v[166:167], v[198:199], s[32:33], v[48:49] op_sel_hi:[1,0,1]
	v_exp_f32_e32 v164, v164
	v_exp_f32_e32 v165, v165
	v_pk_add_f32 v[44:45], v[178:179], v[44:45]
	v_pk_fma_f32 v[168:169], v[202:203], s[32:33], v[48:49] op_sel_hi:[1,0,1]
	v_exp_f32_e32 v166, v166
	v_exp_f32_e32 v167, v167
	v_pk_add_f32 v[44:45], v[164:165], v[44:45]
	v_pk_fma_f32 v[170:171], v[194:195], s[32:33], v[48:49] op_sel_hi:[1,0,1]
	v_exp_f32_e32 v168, v168
	v_exp_f32_e32 v169, v169
	v_pk_add_f32 v[44:45], v[166:167], v[44:45]
	v_pk_fma_f32 v[154:155], v[212:213], s[32:33], v[48:49] op_sel_hi:[1,0,1]
	v_exp_f32_e32 v170, v170
	v_exp_f32_e32 v171, v171
	v_pk_add_f32 v[44:45], v[168:169], v[44:45]
	v_pk_fma_f32 v[156:157], v[210:211], s[32:33], v[48:49] op_sel_hi:[1,0,1]
	v_exp_f32_e32 v154, v154
	v_exp_f32_e32 v155, v155
	v_pk_add_f32 v[44:45], v[170:171], v[44:45]
	v_pk_fma_f32 v[160:161], v[204:205], s[32:33], v[48:49] op_sel_hi:[1,0,1]
	v_exp_f32_e32 v156, v156
	v_exp_f32_e32 v157, v157
	v_pk_add_f32 v[44:45], v[154:155], v[44:45]
	s_nop 0
	v_exp_f32_e32 v160, v160
	v_exp_f32_e32 v161, v161
	v_pk_add_f32 v[44:45], v[156:157], v[44:45]
	s_nop 0
	v_pk_add_f32 v[44:45], v[160:161], v[44:45]
	s_nop 0
	v_add_f32_e32 v44, v44, v45
	v_mov_b32_e32 v48, 0
	v_mov_b32_e32 v45, v44
	s_nop 1
	v_permlane32_swap_b32 v44, v45
	s_nop 1
	s_nop 0
	v_add_f32_e32 v44, v44, v45
	v_mov_b32_e32 v45, v44
	s_nop 1
	v_permlane16_swap_b32 v44, v45
	s_nop 1
	s_nop 0
	v_add_f32_e32 v44, v44, v45
	v_div_scale_f32 v45, s[20:21], v44, v44, 1.0
	v_rcp_f32_e32 v49, v45
	s_nop 0
	v_fma_f32 v140, -v45, v49, 1.0
	v_fmac_f32_e32 v49, v140, v49
	v_div_scale_f32 v140, vcc, 1.0, v44, 1.0
	v_mul_f32_e32 v141, v140, v49
	v_fma_f32 v142, -v45, v141, v140
	v_fmac_f32_e32 v141, v142, v49
	v_fma_f32 v45, -v45, v141, v140
	v_div_fmas_f32 v45, v45, v49, v141
	v_div_fixup_f32 v162, v45, v44, 1.0
	s_waitcnt vmcnt(15)
	ds_write_b128 v252, v[102:105]
	s_waitcnt vmcnt(14)
	ds_write_b128 v252, v[110:113] offset:1152
	s_waitcnt vmcnt(13)
	ds_write_b128 v252, v[126:129] offset:2304
	s_waitcnt vmcnt(12)
	ds_write_b128 v252, v[130:133] offset:3456
	ds_read_u16 v44, v151 offset:256
	ds_read_u16 v45, v151 offset:272
	ds_read_u16 v49, v151 offset:288
	ds_read_u16 v126, v151 offset:304
	s_waitcnt lgkmcnt(0)
	v_lshl_or_b32 v44, v44, 8, v250
	v_lshl_or_b32 v45, v45, 8, v250
	global_load_dwordx4 v[102:105], v44, s[50:51] offset:128
	global_load_dwordx4 v[110:113], v45, s[50:51] offset:128
	v_lshl_or_b32 v44, v49, 8, v250
	v_lshl_or_b32 v45, v126, 8, v250
	global_load_dwordx4 v[126:129], v44, s[50:51] offset:128
	global_load_dwordx4 v[130:133], v45, s[50:51] offset:128
	v_pk_mul_f32 v[44:45], v[162:163], v[46:47] op_sel_hi:[0,1]
	v_pk_mul_f32 v[46:47], v[162:163], v[134:135] op_sel_hi:[0,1]
	v_cvt_pk_bf16_f32 v44, v44, v45
	v_cvt_pk_bf16_f32 v45, v46, v47
	v_pk_mul_f32 v[46:47], v[162:163], v[136:137] op_sel_hi:[0,1]
	v_pk_mul_f32 v[134:135], v[162:163], v[138:139] op_sel_hi:[0,1]
	s_waitcnt lgkmcnt(0)
	v_cvt_pk_bf16_f32 v46, v46, v47
	v_cvt_pk_bf16_f32 v47, v134, v135
	ds_read_b64_tr_b16 v[136:137], v249 offset:2304
	ds_read_b64_tr_b16 v[134:135], v249
	ds_read_b64_tr_b16 v[138:139], v249 offset:32
	ds_read_b64_tr_b16 v[186:187], v249 offset:64
	ds_read_b64_tr_b16 v[190:191], v249 offset:96
	ds_read_b64_tr_b16 v[140:141], v249 offset:2336
	ds_read_b64_tr_b16 v[188:189], v249 offset:2368
	ds_read_b64_tr_b16 v[192:193], v249 offset:2400
	s_waitcnt lgkmcnt(6)
	v_mfma_f32_16x16x32_bf16 v[142:145], v[44:47], v[134:137], 0
	s_waitcnt lgkmcnt(2)
	v_mfma_f32_16x16x32_bf16 v[138:141], v[44:47], v[138:141], 0
	s_waitcnt lgkmcnt(1)
	v_mfma_f32_16x16x32_bf16 v[134:137], v[44:47], v[186:189], 0
	s_waitcnt lgkmcnt(0)
	v_mfma_f32_16x16x32_bf16 v[44:47], v[44:47], v[190:193], 0
	s_waitcnt vmcnt(15)
	ds_write_b128 v252, v[86:89] offset:4608
	s_waitcnt vmcnt(14)
	ds_write_b128 v252, v[94:97] offset:5760
	s_waitcnt vmcnt(13)
	ds_write_b128 v252, v[118:121] offset:6912
	s_waitcnt vmcnt(12)
	ds_write_b128 v252, v[122:125] offset:8064
	ds_read_u16 v49, v151 offset:320
	ds_read_u16 v86, v151 offset:336
	ds_read_u16 v118, v151 offset:352
	ds_read_u16 v119, v151 offset:368
	s_waitcnt lgkmcnt(0)
	v_lshl_or_b32 v49, v49, 8, v250
	v_lshl_or_b32 v94, v86, 8, v250
	global_load_dwordx4 v[86:89], v49, s[50:51] offset:128
	s_nop 0
	global_load_dwordx4 v[94:97], v94, s[50:51] offset:128
	v_lshl_or_b32 v49, v118, 8, v250
	v_lshl_or_b32 v122, v119, 8, v250
	global_load_dwordx4 v[118:121], v49, s[50:51] offset:128
	s_nop 0
	global_load_dwordx4 v[122:125], v122, s[50:51] offset:128
	v_pk_mul_f32 v[186:187], v[162:163], v[226:227] op_sel_hi:[0,1]
	v_pk_mul_f32 v[188:189], v[162:163], v[228:229] op_sel_hi:[0,1]
	v_cvt_pk_bf16_f32 v186, v186, v187
	v_cvt_pk_bf16_f32 v187, v188, v189
	v_pk_mul_f32 v[188:189], v[162:163], v[230:231] op_sel_hi:[0,1]
	v_pk_mul_f32 v[190:191], v[162:163], v[232:233] op_sel_hi:[0,1]
	v_cvt_pk_bf16_f32 v188, v188, v189
	v_cvt_pk_bf16_f32 v189, v190, v191
	s_waitcnt lgkmcnt(0)
	ds_read_b64_tr_b16 v[192:193], v249 offset:6912
	ds_read_b64_tr_b16 v[190:191], v249 offset:4608
	ds_read_b64_tr_b16 v[198:199], v249 offset:4640
	s_waitcnt lgkmcnt(1)
	v_mfma_f32_16x16x32_bf16 v[142:145], v[186:189], v[190:193], v[142:145]
	ds_read_b64_tr_b16 v[200:201], v249 offset:6944
	ds_read_b64_tr_b16 v[190:191], v249 offset:4672
	ds_read_b64_tr_b16 v[192:193], v249 offset:6976
	s_waitcnt lgkmcnt(0)
	v_mfma_f32_16x16x32_bf16 v[134:137], v[186:189], v[190:193], v[134:137]
	ds_read_b64_tr_b16 v[190:191], v249 offset:4704
	ds_read_b64_tr_b16 v[192:193], v249 offset:7008
	v_mfma_f32_16x16x32_bf16 v[138:141], v[186:189], v[198:201], v[138:141]
	s_waitcnt lgkmcnt(0)
	v_mfma_f32_16x16x32_bf16 v[44:47], v[186:189], v[190:193], v[44:47]
	s_waitcnt vmcnt(15)
	ds_write_b128 v252, v[78:81]
	s_waitcnt vmcnt(14)
	ds_write_b128 v252, v[82:85] offset:1152
	s_waitcnt vmcnt(13)
	ds_write_b128 v252, v[106:109] offset:2304
	s_waitcnt vmcnt(12)
	ds_write_b128 v252, v[114:117] offset:3456
	ds_read_u16 v49, v151 offset:384
	ds_read_u16 v78, v151 offset:400
	ds_read_u16 v106, v151 offset:416
	ds_read_u16 v107, v151 offset:432
	s_waitcnt lgkmcnt(0)
	v_lshl_or_b32 v49, v49, 8, v250
	v_lshl_or_b32 v82, v78, 8, v250
	global_load_dwordx4 v[78:81], v49, s[50:51] offset:128
	s_nop 0
	global_load_dwordx4 v[82:85], v82, s[50:51] offset:128
	v_lshl_or_b32 v49, v106, 8, v250
	v_lshl_or_b32 v114, v107, 8, v250
	global_load_dwordx4 v[106:109], v49, s[50:51] offset:128
	s_nop 0
	global_load_dwordx4 v[114:117], v114, s[50:51] offset:128
	v_pk_mul_f32 v[186:187], v[162:163], v[218:219] op_sel_hi:[0,1]
	v_pk_mul_f32 v[188:189], v[162:163], v[220:221] op_sel_hi:[0,1]
	v_cvt_pk_bf16_f32 v186, v186, v187
	v_cvt_pk_bf16_f32 v187, v188, v189
	v_pk_mul_f32 v[188:189], v[162:163], v[222:223] op_sel_hi:[0,1]
	v_pk_mul_f32 v[190:191], v[162:163], v[224:225] op_sel_hi:[0,1]
	v_cvt_pk_bf16_f32 v188, v188, v189
	v_cvt_pk_bf16_f32 v189, v190, v191
	s_waitcnt lgkmcnt(0)
	ds_read_b64_tr_b16 v[192:193], v249 offset:2304
	ds_read_b64_tr_b16 v[190:191], v249
	ds_read_b64_tr_b16 v[198:199], v249 offset:32
	s_waitcnt lgkmcnt(1)
	v_mfma_f32_16x16x32_bf16 v[142:145], v[186:189], v[190:193], v[142:145]
	ds_read_b64_tr_b16 v[200:201], v249 offset:2336
	ds_read_b64_tr_b16 v[190:191], v249 offset:64
	ds_read_b64_tr_b16 v[192:193], v249 offset:2368
	s_waitcnt lgkmcnt(0)
	v_mfma_f32_16x16x32_bf16 v[134:137], v[186:189], v[190:193], v[134:137]
	ds_read_b64_tr_b16 v[190:191], v249 offset:96
	ds_read_b64_tr_b16 v[192:193], v249 offset:2400
	v_mfma_f32_16x16x32_bf16 v[138:141], v[186:189], v[198:201], v[138:141]
	s_waitcnt lgkmcnt(0)
	v_mfma_f32_16x16x32_bf16 v[44:47], v[186:189], v[190:193], v[44:47]
	s_waitcnt vmcnt(15)
	ds_write_b128 v252, v[70:73] offset:4608
	s_waitcnt vmcnt(14)
	ds_write_b128 v252, v[74:77] offset:5760
	s_waitcnt vmcnt(13)
	ds_write_b128 v252, v[90:93] offset:6912
	s_waitcnt vmcnt(12)
	ds_write_b128 v252, v[98:101] offset:8064
	ds_read_u16 v49, v151 offset:448
	ds_read_u16 v70, v151 offset:464
	ds_read_u16 v90, v151 offset:480
	ds_read_u16 v91, v151 offset:496
	s_waitcnt lgkmcnt(0)
	v_lshl_or_b32 v49, v49, 8, v250
	v_lshl_or_b32 v74, v70, 8, v250
	global_load_dwordx4 v[70:73], v49, s[50:51] offset:128
	s_nop 0
	global_load_dwordx4 v[74:77], v74, s[50:51] offset:128
	v_lshl_or_b32 v49, v90, 8, v250
	v_lshl_or_b32 v98, v91, 8, v250
	global_load_dwordx4 v[90:93], v49, s[50:51] offset:128
	s_nop 0
	global_load_dwordx4 v[98:101], v98, s[50:51] offset:128
	v_pk_mul_f32 v[186:187], v[162:163], v[206:207] op_sel_hi:[0,1]
	v_pk_mul_f32 v[188:189], v[162:163], v[208:209] op_sel_hi:[0,1]
	v_cvt_pk_bf16_f32 v186, v186, v187
	v_cvt_pk_bf16_f32 v187, v188, v189
	v_pk_mul_f32 v[188:189], v[162:163], v[214:215] op_sel_hi:[0,1]
	v_pk_mul_f32 v[190:191], v[162:163], v[216:217] op_sel_hi:[0,1]
	v_cvt_pk_bf16_f32 v188, v188, v189
	v_cvt_pk_bf16_f32 v189, v190, v191
	s_waitcnt lgkmcnt(0)
	ds_read_b64_tr_b16 v[192:193], v249 offset:6912
	ds_read_b64_tr_b16 v[190:191], v249 offset:4608
	ds_read_b64_tr_b16 v[198:199], v249 offset:4640
	s_waitcnt lgkmcnt(1)
	v_mfma_f32_16x16x32_bf16 v[142:145], v[186:189], v[190:193], v[142:145]
	ds_read_b64_tr_b16 v[200:201], v249 offset:6944
	ds_read_b64_tr_b16 v[190:191], v249 offset:4672
	ds_read_b64_tr_b16 v[192:193], v249 offset:6976
	s_waitcnt lgkmcnt(0)
	v_mfma_f32_16x16x32_bf16 v[134:137], v[186:189], v[190:193], v[134:137]
	ds_read_b64_tr_b16 v[190:191], v249 offset:4704
	ds_read_b64_tr_b16 v[192:193], v249 offset:7008
	v_mfma_f32_16x16x32_bf16 v[138:141], v[186:189], v[198:201], v[138:141]
	s_waitcnt lgkmcnt(0)
	v_mfma_f32_16x16x32_bf16 v[44:47], v[186:189], v[190:193], v[44:47]
	v_pk_mul_f32 v[182:183], v[162:163], v[182:183] op_sel_hi:[0,1]
	v_pk_mul_f32 v[180:181], v[162:163], v[180:181] op_sel_hi:[0,1]
	v_cvt_pk_bf16_f32 v182, v182, v183
	v_cvt_pk_bf16_f32 v183, v180, v181
	v_pk_mul_f32 v[180:181], v[162:163], v[184:185] op_sel_hi:[0,1]
	s_waitcnt vmcnt(15)
	ds_write_b128 v252, v[102:105]
	s_waitcnt vmcnt(14)
	ds_write_b128 v252, v[110:113] offset:1152
	s_waitcnt vmcnt(13)
	ds_write_b128 v252, v[126:129] offset:2304
	s_waitcnt vmcnt(12)
	ds_write_b128 v252, v[130:133] offset:3456
	v_cvt_pk_bf16_f32 v184, v180, v181
	v_pk_mul_f32 v[180:181], v[162:163], v[196:197] op_sel_hi:[0,1]
	v_cvt_pk_bf16_f32 v185, v180, v181
	s_waitcnt lgkmcnt(0)
	ds_read_b64_tr_b16 v[188:189], v249 offset:2304
	ds_read_b64_tr_b16 v[186:187], v249
	ds_read_b64_tr_b16 v[190:191], v249 offset:32
	s_waitcnt lgkmcnt(1)
	v_mfma_f32_16x16x32_bf16 v[142:145], v[182:185], v[186:189], v[142:145]
	ds_read_b64_tr_b16 v[192:193], v249 offset:2336
	ds_read_b64_tr_b16 v[186:187], v249 offset:64
	ds_read_b64_tr_b16 v[188:189], v249 offset:2368
	s_waitcnt lgkmcnt(0)
	v_mfma_f32_16x16x32_bf16 v[134:137], v[182:185], v[186:189], v[134:137]
	ds_read_b64_tr_b16 v[186:187], v249 offset:96
	ds_read_b64_tr_b16 v[188:189], v249 offset:2400
	v_mfma_f32_16x16x32_bf16 v[138:141], v[182:185], v[190:193], v[138:141]
	s_waitcnt lgkmcnt(0)
	v_mfma_f32_16x16x32_bf16 v[44:47], v[182:185], v[186:189], v[44:47]
	v_pk_mul_f32 v[172:173], v[162:163], v[172:173] op_sel_hi:[0,1]
	v_pk_mul_f32 v[174:175], v[162:163], v[174:175] op_sel_hi:[0,1]
	s_waitcnt vmcnt(11)
	ds_write_b128 v252, v[86:89] offset:4608
	s_waitcnt vmcnt(10)
	ds_write_b128 v252, v[94:97] offset:5760
	s_waitcnt vmcnt(9)
	ds_write_b128 v252, v[118:121] offset:6912
	s_waitcnt vmcnt(8)
	ds_write_b128 v252, v[122:125] offset:8064
	v_cvt_pk_bf16_f32 v172, v172, v173
	v_cvt_pk_bf16_f32 v173, v174, v175
	v_pk_mul_f32 v[174:175], v[162:163], v[176:177] op_sel_hi:[0,1]
	v_pk_mul_f32 v[176:177], v[162:163], v[178:179] op_sel_hi:[0,1]
	v_cvt_pk_bf16_f32 v174, v174, v175
	v_cvt_pk_bf16_f32 v175, v176, v177
	s_waitcnt lgkmcnt(0)
	ds_read_b64_tr_b16 v[178:179], v249 offset:6912
	ds_read_b64_tr_b16 v[176:177], v249 offset:4608
	ds_read_b64_tr_b16 v[180:181], v249 offset:4640
	s_waitcnt lgkmcnt(1)
	v_mfma_f32_16x16x32_bf16 v[142:145], v[172:175], v[176:179], v[142:145]
	ds_read_b64_tr_b16 v[182:183], v249 offset:6944
	ds_read_b64_tr_b16 v[176:177], v249 offset:4672
	ds_read_b64_tr_b16 v[178:179], v249 offset:6976
	s_waitcnt lgkmcnt(0)
	v_mfma_f32_16x16x32_bf16 v[134:137], v[172:175], v[176:179], v[134:137]
	ds_read_b64_tr_b16 v[176:177], v249 offset:4704
	ds_read_b64_tr_b16 v[178:179], v249 offset:7008
	v_mfma_f32_16x16x32_bf16 v[138:141], v[172:175], v[180:183], v[138:141]
	s_waitcnt lgkmcnt(0)
	v_mfma_f32_16x16x32_bf16 v[44:47], v[172:175], v[176:179], v[44:47]
	v_pk_mul_f32 v[164:165], v[162:163], v[164:165] op_sel_hi:[0,1]
	v_pk_mul_f32 v[166:167], v[162:163], v[166:167] op_sel_hi:[0,1]
	s_waitcnt vmcnt(7)
	ds_write_b128 v252, v[78:81]
	s_waitcnt vmcnt(6)
	ds_write_b128 v252, v[82:85] offset:1152
	s_waitcnt vmcnt(5)
	ds_write_b128 v252, v[106:109] offset:2304
	s_waitcnt vmcnt(4)
	ds_write_b128 v252, v[114:117] offset:3456
	v_cvt_pk_bf16_f32 v164, v164, v165
	v_cvt_pk_bf16_f32 v165, v166, v167
	v_pk_mul_f32 v[166:167], v[162:163], v[168:169] op_sel_hi:[0,1]
	v_pk_mul_f32 v[168:169], v[162:163], v[170:171] op_sel_hi:[0,1]
	v_cvt_pk_bf16_f32 v166, v166, v167
	v_cvt_pk_bf16_f32 v167, v168, v169
	s_waitcnt lgkmcnt(0)
	ds_read_b64_tr_b16 v[170:171], v249 offset:2304
	ds_read_b64_tr_b16 v[168:169], v249
	ds_read_b64_tr_b16 v[172:173], v249 offset:32
	s_waitcnt lgkmcnt(1)
	v_mfma_f32_16x16x32_bf16 v[142:145], v[164:167], v[168:171], v[142:145]
	ds_read_b64_tr_b16 v[174:175], v249 offset:2336
	ds_read_b64_tr_b16 v[168:169], v249 offset:64
	ds_read_b64_tr_b16 v[170:171], v249 offset:2368
	s_waitcnt lgkmcnt(0)
	v_mfma_f32_16x16x32_bf16 v[134:137], v[164:167], v[168:171], v[134:137]
	ds_read_b64_tr_b16 v[168:169], v249 offset:96
	ds_read_b64_tr_b16 v[170:171], v249 offset:2400
	v_mfma_f32_16x16x32_bf16 v[138:141], v[164:167], v[172:175], v[138:141]
	s_waitcnt lgkmcnt(0)
	v_mfma_f32_16x16x32_bf16 v[44:47], v[164:167], v[168:171], v[44:47]
	v_pk_mul_f32 v[154:155], v[162:163], v[154:155] op_sel_hi:[0,1]
	v_pk_mul_f32 v[156:157], v[162:163], v[156:157] op_sel_hi:[0,1]
	s_waitcnt vmcnt(3)
	ds_write_b128 v252, v[70:73] offset:4608
	s_waitcnt vmcnt(2)
	ds_write_b128 v252, v[74:77] offset:5760
	s_waitcnt vmcnt(1)
	ds_write_b128 v252, v[90:93] offset:6912
	s_waitcnt vmcnt(0)
	ds_write_b128 v252, v[98:101] offset:8064
	v_cvt_pk_bf16_f32 v154, v154, v155
	v_cvt_pk_bf16_f32 v155, v156, v157
	v_pk_mul_f32 v[156:157], v[162:163], v[158:159] op_sel_hi:[0,1]
	v_pk_mul_f32 v[158:159], v[162:163], v[160:161] op_sel_hi:[0,1]
	v_cvt_pk_bf16_f32 v156, v156, v157
	v_cvt_pk_bf16_f32 v157, v158, v159
	s_waitcnt lgkmcnt(0)
	ds_read_b64_tr_b16 v[160:161], v249 offset:6912
	ds_read_b64_tr_b16 v[158:159], v249 offset:4608
	ds_read_b64_tr_b16 v[162:163], v249 offset:4640
	s_waitcnt lgkmcnt(1)
	v_mfma_f32_16x16x32_bf16 v[142:145], v[154:157], v[158:161], v[142:145]
	ds_read_b64_tr_b16 v[164:165], v249 offset:6944
	ds_read_b64_tr_b16 v[158:159], v249 offset:4672
	ds_read_b64_tr_b16 v[160:161], v249 offset:6976
	s_waitcnt lgkmcnt(0)
	v_mfma_f32_16x16x32_bf16 v[134:137], v[154:157], v[158:161], v[134:137]
	ds_read_b64_tr_b16 v[158:159], v249 offset:4704
	ds_read_b64_tr_b16 v[160:161], v249 offset:7008
	v_mfma_f32_16x16x32_bf16 v[138:141], v[154:157], v[162:165], v[138:141]
	s_waitcnt lgkmcnt(0)
	v_mfma_f32_16x16x32_bf16 v[44:47], v[154:157], v[158:161], v[44:47]
	s_waitcnt lgkmcnt(0)
	s_and_saveexec_b64 s[8:9], s[40:41]
	s_cbranch_execz .LBB0_784
	s_lshl_b64 s[18:19], s[52:53], 10
	v_lshl_add_u64 v[154:155], v[148:149], 0, s[18:19]
	v_cvt_pk_bf16_f32 v49, v142, v143
	global_store_short v[154:155], v49, off
	global_store_short_d16_hi v[154:155], v49, off offset:128
	v_cvt_pk_bf16_f32 v49, v144, v145
	global_store_short v[154:155], v49, off offset:256
	global_store_short_d16_hi v[154:155], v49, off offset:384
	v_cvt_pk_bf16_f32 v49, v138, v139
	global_store_short v[154:155], v49, off offset:32
	global_store_short_d16_hi v[154:155], v49, off offset:160
	v_cvt_pk_bf16_f32 v49, v140, v141
	global_store_short v[154:155], v49, off offset:288
	global_store_short_d16_hi v[154:155], v49, off offset:416
	v_cvt_pk_bf16_f32 v49, v134, v135
	global_store_short v[154:155], v49, off offset:64
	global_store_short_d16_hi v[154:155], v49, off offset:192
	v_cvt_pk_bf16_f32 v49, v136, v137
	global_store_short v[154:155], v49, off offset:320
	global_store_short_d16_hi v[154:155], v49, off offset:448
	v_cvt_pk_bf16_f32 v49, v44, v45
	global_store_short v[154:155], v49, off offset:96
	global_store_short_d16_hi v[154:155], v49, off offset:224
	v_cvt_pk_bf16_f32 v49, v46, v47
	global_store_short v[154:155], v49, off offset:352
	global_store_short_d16_hi v[154:155], v49, off offset:480
	s_branch .LBB0_784
